# kargfirst
# speedup vs baseline: 1.0189x; 1.0189x over previous
_Z11prep_kernelPKfS0_PKiS2_S0_S0_S0_S0_S0_S0_Pc:
	s_load_dwordx4 s[28:31], s[0:1], 0x40
	s_load_dwordx8 s[12:19], s[0:1], 0x0
	s_load_dwordx8 s[20:27], s[0:1], 0x20
	s_load_dwordx2 s[32:33], s[0:1], 0x50
	s_load_dword s40, s[0:1], 0x80
	s_getpc_b64 s[36:37]
	s_add_u32 s36, s36, _Z11attn_kernelILi4EEvPKfS1_S1_S1_S1_S1_PKcPf@rel32@lo+4
	s_addc_u32 s37, s37, _Z11attn_kernelILi4EEvPKfS1_S1_S1_S1_S1_PKcPf@rel32@hi+12
	v_and_b32_e32 v192, 63, v0
	v_lshlrev_b32_e32 v192, 7, v192
	v_min_u32_e32 v192, 0x1180, v192
	global_load_dword v192, v192, s[36:37]
	s_lshr_b32 s4, s2, 2
	v_lshrrev_b32_e32 v2, 6, v0
	s_and_b32 s4, s4, 0x1ffffffe
	v_and_b32_e32 v1, 15, v0
	s_and_b32 s3, s2, 7
	v_or_b32_e32 v2, s4, v2
	v_lshl_or_b32 v88, v2, 3, s3
	v_cmp_gt_u32_e64 s[10:11], 14, v1
	v_mul_lo_u32 v7, v88, 14
	v_and_b32_e32 v105, 63, v0
	v_cndmask_b32_e64 v6, 13, v1, s[10:11]
	v_add_u32_e32 v2, v7, v6
	v_mul_u32_u24_e32 v4, 12, v2
	v_lshlrev_b32_e32 v5, 2, v6
	v_cmp_gt_u32_e64 s[8:9], 48, v105
	v_cmp_gt_u32_e64 s[6:7], 14, v105
	v_lshlrev_b32_e32 v118, 1, v0
	v_lshrrev_b32_e32 v104, 4, v0
	v_cndmask_b32_e64 v8, 0, v105, s[8:9]
	v_cndmask_b32_e64 v9, 0, v105, s[6:7]
	v_mad_u32_u24 v8, v88, 48, v8
	v_add_lshl_u32 v9, v7, v9, 2
	v_lshlrev_b32_e32 v8, 2, v8
	s_lshl_b32 s2, s2, 3
	s_and_b32 s2, s2, 0x78
	v_and_b32_e32 v106, 30, v118
	v_or_b32_e32 v107, s2, v104
	v_cmp_gt_u32_e64 s[2:3], 23, v106
	v_or_b32_e32 v10, 1, v106
	v_cmp_gt_u32_e64 s[4:5], 23, v10
	v_lshlrev_b32_e32 v11, 7, v106
	v_lshlrev_b32_e32 v10, 7, v10
	v_cndmask_b32_e64 v11, 0, v11, s[2:3]
	v_cndmask_b32_e64 v10, 0, v10, s[4:5]
	v_or_b32_e32 v11, v11, v107
	v_or_b32_e32 v10, v10, v107
	v_lshlrev_b32_e32 v11, 2, v11
	v_lshlrev_b32_e32 v10, 2, v10
	v_lshlrev_b32_e32 v12, 2, v107
	v_lshlrev_b32_e32 v119, 5, v0
	v_lshlrev_b32_e32 v13, 2, v0
	v_and_b32_e32 v109, 12, v13
	v_and_b32_e32 v91, 0xf80, v119
	v_lshl_or_b32 v91, v109, 2, v91
	v_or_b32_e32 v92, 0x1000, v91
	v_lshlrev_b32_e32 v90, 9, v2
	v_and_b32_e32 v16, 48, v0
	v_or_b32_e32 v90, v90, v16
	v_or_b32_e32 v112, 0x80, v0
	v_or_b32_e32 v111, 0x180, v0
	v_or_b32_e32 v108, 0x280, v0
	v_mov_b32_e32 v87, 0
	v_bfe_u32 v110, v0, 4, 2
	s_movk_i32 s34, 0x60
	v_lshrrev_b32_e32 v136, 1, v0
	v_lshrrev_b32_e32 v18, 3, v0
	v_and_b32_e32 v18, 4, v18
	v_and_b32_e32 v19, 24, v0
	v_and_b32_e32 v20, 2, v136
	v_or3_b32 v18, v18, v19, v20
	v_and_or_b32 v136, v136, s34, v18
	v_mul_u32_u24_e32 v18, 0x110, v109
	v_lshl_add_u32 v136, v136, 1, v18
	v_add_u32_e32 v137, 0x1100, v136
	v_add_u32_e32 v138, 0x2200, v136
	v_lshlrev_b32_e32 v18, 9, v88
	v_and_b32_e32 v19, 0x100, v119
	v_lshlrev_b32_e32 v20, 4, v0
	v_and_b32_e32 v20, 48, v20
	v_or3_b32 v139, v18, v19, v20
	v_and_b32_e32 v19, 8, v118
	v_and_b32_e32 v20, 64, v118
	v_or3_b32 v139, v139, v19, v20
	v_lshlrev_b32_e32 v19, 2, v110
	v_and_b32_e32 v20, 4, v19
	v_or_b32_e32 v139, v139, v20
	v_lshl_or_b32 v140, v1, 5, v18
	v_or_b32_e32 v140, v140, v19
	v_add_u32_e32 v140, 0x80000, v140
	v_lshl_or_b32 v141, v88, 4, v1
	v_lshlrev_b32_e32 v141, 3, v141
	v_add_u32_e32 v141, 0x140000, v141
	v_lshlrev_b32_e32 v20, 8, v88
	v_mul_u32_u24_e32 v21, 43, v105
	v_lshrrev_b32_e32 v21, 9, v21
	v_mul_u32_u24_e32 v21, 12, v21
	v_sub_u32_e32 v22, v105, v21
	v_and_b32_e32 v142, 3, v22
	v_lshrrev_b32_e32 v22, 2, v22
	v_mad_u32_u24 v142, v142, 3, v22
	v_add_u32_e32 v142, v142, v21
	v_lshl_add_u32 v142, v142, 2, v20
	v_add_u32_e32 v142, 0x164000, v142
	v_lshl_add_u32 v143, v105, 2, v20
	v_add_u32_e32 v143, 0x164000, v143
	v_lshlrev_b32_e32 v123, 6, v107
	v_lshl_add_u32 v123, v106, 1, v123
	v_add_u32_e32 v123, 0x160000, v123
	v_lshl_add_u32 v122, v1, 4, v20
	v_or_b32_e32 v122, v122, v19
	v_add_u32_e32 v122, 0x100000, v122
	s_waitcnt lgkmcnt(0)
	global_load_dwordx3 v[82:84], v4, s[12:13]
	global_load_dword v85, v5, s[26:27]
	global_load_dword v114, v8, s[18:19]
	global_load_dword v115, v9, s[16:17]
	global_load_dword v116, v11, s[28:29]
	global_load_dword v113, v10, s[28:29]
	global_load_dword v117, v12, s[30:31]
	global_load_dwordx4 v[66:69], v91, s[20:21]
	global_load_dwordx4 v[70:73], v91, s[20:21] offset:64
	global_load_dwordx4 v[74:77], v92, s[20:21]
	global_load_dwordx4 v[78:81], v92, s[20:21] offset:64
	global_load_dwordx4 v[58:61], v91, s[22:23]
	global_load_dwordx4 v[62:65], v91, s[22:23] offset:64
	global_load_dwordx4 v[50:53], v92, s[22:23]
	global_load_dwordx4 v[54:57], v92, s[22:23] offset:64
	global_load_dwordx4 v[42:45], v91, s[24:25]
	global_load_dwordx4 v[46:49], v91, s[24:25] offset:64
	global_load_dwordx4 v[34:37], v92, s[24:25]
	global_load_dwordx4 v[38:41], v92, s[24:25] offset:64
	global_load_dwordx4 v[26:29], v90, s[14:15] nt
	global_load_dwordx4 v[30:33], v90, s[14:15] offset:64 nt
	global_load_dwordx4 v[18:21], v90, s[14:15] offset:128 nt
	global_load_dwordx4 v[22:25], v90, s[14:15] offset:192 nt
	global_load_dwordx4 v[10:13], v90, s[14:15] offset:256 nt
	global_load_dwordx4 v[14:17], v90, s[14:15] offset:320 nt
	global_load_dwordx4 v[2:5], v90, s[14:15] offset:384 nt
	global_load_dwordx4 v[6:9], v90, s[14:15] offset:448 nt
	s_waitcnt vmcnt(26)
	v_mov_b32_e32 v90, v83
	v_mov_b32_e32 v91, v84
	v_lshlrev_b32_e32 v86, 2, v110
	s_waitcnt vmcnt(25)
	v_mul_f32_e32 v84, 0x3fb8aa3b, v85
	s_mov_b32 s14, 0x41700000
	v_exp_f32_e32 v84, v84
	v_cndmask_b32_e64 v94, 0, 1.0, s[10:11]
	v_add_f32_e32 v84, 1.0, v84
	v_cmp_lt_f32_e32 vcc, s14, v85
	v_log_f32_e32 v84, v84
	v_cmp_lt_u32_e64 s[12:13], 15, v105
	v_mul_f32_e32 v84, 0x3f317218, v84
	v_cndmask_b32_e32 v84, v84, v85, vcc
	v_mul_f32_e32 v84, 0xbe715bef, v84
	v_mul_f32_e32 v84, 0x3f3504f3, v84
	v_mul_f32_e32 v84, 0x41800000, v84
	v_cndmask_b32_e64 v99, 0, v84, s[10:11]
	v_mul_f32_e32 v101, -2.0, v99
	v_mul_f32_e32 v100, v82, v82
	v_cmp_gt_u32_e32 vcc, 16, v105
	v_fmac_f32_e32 v100, v90, v90
	v_cmp_eq_u32_e64 s[12:13], 0, v110
	v_fmac_f32_e32 v100, v91, v91
	v_cmp_eq_u32_e64 s[14:15], 1, v110
	v_mul_f32_e32 v83, v101, v82
	v_cmp_eq_u32_e64 s[16:17], 2, v110
	v_mul_f32_e32 v84, v101, v90
	v_mul_f32_e32 v85, v101, v91
	v_mul_f32_e32 v89, v99, v100
	v_mul_f32_e32 v92, v82, v94
	v_mul_f32_e32 v93, v90, v94
	v_mul_f32_e32 v95, v91, v94
	v_mul_f32_e32 v96, v100, v94
	v_cvt_pk_fp8_f32 v88, v83, v83
	v_cvt_pk_fp8_f32 v104, v84, v84
	v_cvt_f32_fp8_e32 v97, v88
	v_cvt_f32_fp8_e32 v98, v104
	v_sub_f32_e32 v97, v83, v97
	v_sub_f32_e32 v98, v84, v98
	v_cvt_pk_fp8_f32 v88, v85, v85
	v_cvt_pk_fp8_f32 v104, v99, v99
	v_cvt_f32_fp8_e32 v101, v88
	v_cvt_f32_fp8_e32 v102, v104
	v_sub_f32_e32 v101, v85, v101
	v_sub_f32_e32 v102, v99, v102
	v_cvt_pk_fp8_f32 v88, v89, v89
	v_cvt_pk_fp8_f32 v104, v92, v92
	v_cvt_f32_fp8_e32 v103, v88
	v_cvt_f32_fp8_e32 v120, v104
	v_sub_f32_e32 v103, v89, v103
	v_sub_f32_e32 v120, v92, v120
	v_cvt_pk_fp8_f32 v88, v93, v93
	v_cvt_pk_fp8_f32 v104, v95, v95
	v_cvt_f32_fp8_e32 v121, v88
	v_cvt_f32_fp8_e32 v86, v104
	v_sub_f32_e32 v121, v93, v121
	v_sub_f32_e32 v86, v95, v86
	v_cvt_pk_fp8_f32 v88, v96, v96
	s_nop 0
	v_cvt_f32_fp8_e32 v87, v88
	s_nop 0
	v_sub_f32_e32 v87, v96, v87
	v_cndmask_b32_e64 v124, v89, v85, s[16:17]
	v_cndmask_b32_e64 v124, v124, v98, s[14:15]
	v_cndmask_b32_e64 v124, v124, v83, s[12:13]
	v_cndmask_b32_e64 v125, v103, v99, s[16:17]
	v_cndmask_b32_e64 v125, v125, v84, s[14:15]
	v_cndmask_b32_e64 v125, v125, v97, s[12:13]
	v_cndmask_b32_e64 v126, 0, v102, s[16:17]
	v_cndmask_b32_e64 v126, v126, v85, s[14:15]
	v_cndmask_b32_e64 v126, v126, v83, s[12:13]
	v_cndmask_b32_e64 v127, 0, v99, s[16:17]
	v_cndmask_b32_e64 v127, v127, v101, s[14:15]
	v_cndmask_b32_e64 v127, v127, v84, s[12:13]
	v_cndmask_b32_e64 v128, v94, v86, s[16:17]
	v_cndmask_b32_e64 v128, v128, v93, s[14:15]
	v_cndmask_b32_e64 v128, v128, v92, s[12:13]
	v_cndmask_b32_e64 v129, v94, v96, s[16:17]
	v_cndmask_b32_e64 v129, v129, v121, s[14:15]
	v_cndmask_b32_e64 v129, v129, v92, s[12:13]
	v_cndmask_b32_e64 v130, 0, v96, s[16:17]
	v_cndmask_b32_e64 v130, v130, v95, s[14:15]
	v_cndmask_b32_e64 v130, v130, v120, s[12:13]
	v_cndmask_b32_e64 v131, 0, v87, s[16:17]
	v_cndmask_b32_e64 v131, v131, v95, s[14:15]
	v_cndmask_b32_e64 v131, v131, v93, s[12:13]
	v_cvt_pk_fp8_f32 v119, v124, v125
	v_cvt_pk_fp8_f32 v103, v128, v129
	v_cvt_pk_fp8_f32 v119, v126, v127 op_sel:[0,0,1]
	v_cvt_pk_fp8_f32 v103, v130, v131 op_sel:[0,0,1]
	s_nop 0
	global_store_dword v139, v119, s[32:33] offset:128
	global_store_dword v140, v103, s[32:33] offset:16
	s_and_saveexec_b64 s[0:1], vcc
	s_cbranch_execz .LBB0_14
	v_cvt_f16_f32_e32 v83, v82
	v_cvt_pk_f16_f32 v90, v90, v91
	s_nop 0
	v_alignbit_b32 v91, 0, v90, 16
	v_pack_b32_f16 v90, v83, v90
	global_store_dwordx2 v141, v[90:91], s[32:33]
